# flush and barrier-wait conversion by waves 1-5 (was 1-4 waits, 1-7 flush)
# speedup vs baseline: 1.0134x; 1.0134x over previous
; __device__ __forceinline__ void xcd_barrier_cv(const XcdBarrier& b, const CvWork& w) {
;     asm volatile("s_waitcnt vmcnt(0)" ::: "memory");
;     const unsigned g0 = w.rel[0];
;     __syncthreads();
;     if (b.wave == 0) {
;         xb_wave0(b, w.rel + 1, g0 + 1u);
;         w.rel[0] = g0 + 1u;
;     } else if (b.wave != 0) {
;         unsigned guard = 0;
;         while (w.rel[0] == g0) { if (w.rel[1] == g0 + 1u || b.wave > 4) { __builtin_amdgcn_s_sleep(1); continue; }
;             if (!cv_one(w)) __builtin_amdgcn_s_sleep(4); if (++guard > (1u << 22)) break; }
.LBB0_193:
	s_add_i32 s0, 0, 0x20170
	s_waitcnt vmcnt(0)
	s_waitcnt vmcnt(16)
	v_mov_b32_e32 v0, s0
	ds_read_b32 v2, v0
	s_cmp_eq_u32 s89, 0
	s_waitcnt lgkmcnt(0)
	s_barrier
	s_cbranch_scc1 .LBB0_219
	v_mov_b32_e32 v0, s0
	ds_read_b32 v0, v0
	s_waitcnt lgkmcnt(0)
	v_cmp_ne_u32_e32 vcc, v0, v2
	s_cbranch_vccnz .LBB0_218
	s_cmp_gt_i32 s89, 5
	s_cselect_b64 s[0:1], -1, 0
	s_lshl_b32 s2, s89, 3
	s_add_i32 s3, 0, 0x20174
	s_add_i32 s10, s2, 0
	v_add_u32_e32 v3, 1, v2
	s_mov_b32 s28, 0
	s_waitcnt vmcnt(15)
	v_mov_b32_e32 v4, s3
	s_add_i32 s2, s10, 0x20180
	v_mov_b32_e32 v1, 0
	s_mov_b32 s3, 0x10000
	v_mov_b32_e32 v5, 0x10001
	s_add_i32 s10, s10, 0x20184
	s_movk_i32 s11, 0x4000
	s_mov_b32 s12, 0x8000
	s_mov_b32 s13, 0xc000
	s_mov_b32 s14, 0x14000
	s_mov_b32 s15, 0x18000
	s_mov_b32 s16, 0x1c000
	s_mov_b32 s17, 0x20000
	s_mov_b32 s18, 0x24000
	s_mov_b32 s19, 0x28000
	s_mov_b32 s20, 0x2c000
	s_mov_b32 s21, 0x30000
	s_mov_b32 s22, 0x34000
	s_mov_b32 s23, 0x38000
	s_mov_b32 s24, 0x3c000
	s_mov_b32 s25, 0xc3e00000
	s_movk_i32 s26, 0x1000
	s_add_i32 s27, 0, 0x20170
	v_mov_b32_e32 v6, 0x43e00000
	s_branch .LBB0_197

; __device__ __forceinline__ void xcd_barrier_cv(const XcdBarrier& b, const CvWork& w) {
;     asm volatile("s_waitcnt vmcnt(0)" ::: "memory");
;     const unsigned g0 = w.rel[0];
;     __syncthreads();
;     if (b.wave == 0) {
;         xb_wave0(b, w.rel + 1, g0 + 1u);
;         w.rel[0] = g0 + 1u;
;     } else if (b.wave != 0) {
;         unsigned guard = 0;
;         while (w.rel[0] == g0) { if (w.rel[1] == g0 + 1u || b.wave > 4) { __builtin_amdgcn_s_sleep(1); continue; }
;             if (!cv_one(w)) __builtin_amdgcn_s_sleep(4); if (++guard > (1u << 22)) break; }
.LBB0_359:
	s_cmp_lt_i32 s81, 3
	s_cbranch_scc1 .LBB0_431
	s_add_i32 s0, 0, 0x20170
	s_waitcnt vmcnt(0)
	v_mov_b32_e32 v0, s0
	ds_read_b32 v2, v0
	s_cmp_eq_u32 s89, 0
	s_waitcnt vmcnt(0) lgkmcnt(0)
	s_barrier
	s_cbranch_scc1 .LBB0_386
	v_mov_b32_e32 v0, s0
	ds_read_b32 v0, v0
	s_waitcnt lgkmcnt(0)
	v_cmp_ne_u32_e32 vcc, v0, v2
	s_cbranch_vccnz .LBB0_385
	s_cmp_gt_i32 s89, 5
	s_cselect_b64 s[0:1], -1, 0
	s_lshl_b32 s2, s89, 3
	s_add_i32 s3, 0, 0x20174
	s_add_i32 s10, s2, 0
	v_add_u32_e32 v3, 1, v2
	s_mov_b32 s28, 0
	v_mov_b32_e32 v4, s3
	s_add_i32 s2, s10, 0x20180
	v_mov_b32_e32 v1, 0
	s_mov_b32 s3, 0x10000
	v_mov_b32_e32 v5, 0x10001
	s_add_i32 s10, s10, 0x20184
	s_movk_i32 s11, 0x4000
	s_mov_b32 s12, 0x8000
	s_mov_b32 s13, 0xc000
	s_mov_b32 s14, 0x14000
	s_mov_b32 s15, 0x18000
	s_mov_b32 s16, 0x1c000
	s_mov_b32 s17, 0x20000
	s_mov_b32 s18, 0x24000
	s_mov_b32 s19, 0x28000
	s_mov_b32 s20, 0x2c000
	s_mov_b32 s21, 0x30000
	s_mov_b32 s22, 0x34000
	s_mov_b32 s23, 0x38000
	s_mov_b32 s24, 0x3c000
	s_mov_b32 s25, 0xc3e00000
	s_movk_i32 s26, 0x1000
	s_add_i32 s27, 0, 0x20170
	v_mov_b32_e32 v6, 0x43e00000
	s_branch .LBB0_364

; __device__ __forceinline__ void xcd_barrier_cv(const XcdBarrier& b, const CvWork& w) {
;     asm volatile("s_waitcnt vmcnt(0)" ::: "memory");
;     const unsigned g0 = w.rel[0];
;     __syncthreads();
;     if (b.wave == 0) {
;         xb_wave0(b, w.rel + 1, g0 + 1u);
;         w.rel[0] = g0 + 1u;
;     } else if (b.wave != 0) {
;         unsigned guard = 0;
;         while (w.rel[0] == g0) { if (w.rel[1] == g0 + 1u || b.wave > 4) { __builtin_amdgcn_s_sleep(1); continue; }
;             if (!cv_one(w)) __builtin_amdgcn_s_sleep(4); if (++guard > (1u << 22)) break; }
.LBB0_479:
	s_cmp_gt_i32 s81, 3
	s_cbranch_scc0 .LBB0_551
	s_add_i32 s0, 0, 0x20170
	s_waitcnt vmcnt(0)
	v_mov_b32_e32 v0, s0
	ds_read_b32 v2, v0
	s_cmp_eq_u32 s89, 0
	s_waitcnt vmcnt(0) lgkmcnt(0)
	s_barrier
	s_cbranch_scc1 .LBB0_506
	v_mov_b32_e32 v0, s0
	ds_read_b32 v0, v0
	s_waitcnt lgkmcnt(0)
	v_cmp_ne_u32_e32 vcc, v0, v2
	s_cbranch_vccnz .LBB0_505
	s_cmp_gt_i32 s89, 5
	s_cselect_b64 s[0:1], -1, 0
	s_lshl_b32 s2, s89, 3
	s_add_i32 s3, 0, 0x20174
	s_add_i32 s10, s2, 0
	v_add_u32_e32 v3, 1, v2
	s_mov_b32 s28, 0
	v_mov_b32_e32 v4, s3
	s_add_i32 s2, s10, 0x20180
	v_mov_b32_e32 v1, 0
	s_mov_b32 s3, 0x10000
	v_mov_b32_e32 v5, 0x10001
	s_add_i32 s10, s10, 0x20184
	s_movk_i32 s11, 0x4000
	s_mov_b32 s12, 0x8000
	s_mov_b32 s13, 0xc000
	s_mov_b32 s14, 0x14000
	s_mov_b32 s15, 0x18000
	s_mov_b32 s16, 0x1c000
	s_mov_b32 s17, 0x20000
	s_mov_b32 s18, 0x24000
	s_mov_b32 s19, 0x28000
	s_mov_b32 s20, 0x2c000
	s_mov_b32 s21, 0x30000
	s_mov_b32 s22, 0x34000
	s_mov_b32 s23, 0x38000
	s_mov_b32 s24, 0x3c000
	s_mov_b32 s25, 0xc3e00000
	s_movk_i32 s26, 0x1000
	s_add_i32 s27, 0, 0x20170
	v_mov_b32_e32 v6, 0x43e00000
	s_branch .LBB0_484

; __device__ __forceinline__ void xcd_barrier_cv(const XcdBarrier& b, const CvWork& w) {
;     asm volatile("s_waitcnt vmcnt(0)" ::: "memory");
;     const unsigned g0 = w.rel[0];
;     __syncthreads();
;     if (b.wave == 0) {
;         xb_wave0(b, w.rel + 1, g0 + 1u);
;         w.rel[0] = g0 + 1u;
;     } else if (b.wave != 0) {
;         unsigned guard = 0;
;         while (w.rel[0] == g0) { if (w.rel[1] == g0 + 1u || b.wave > 4) { __builtin_amdgcn_s_sleep(1); continue; }
;             if (!cv_one(w)) __builtin_amdgcn_s_sleep(4); if (++guard > (1u << 22)) break; }
.LBB0_643:
	s_cmp_lt_i32 s81, 5
	s_cbranch_scc1 .LBB0_715
	s_add_i32 s0, 0, 0x20170
	s_waitcnt vmcnt(0)
	v_mov_b32_e32 v0, s0
	ds_read_b32 v2, v0
	s_cmp_eq_u32 s89, 0
	s_waitcnt vmcnt(0) lgkmcnt(0)
	s_barrier
	s_cbranch_scc1 .LBB0_670
	v_mov_b32_e32 v0, s0
	ds_read_b32 v0, v0
	s_waitcnt lgkmcnt(0)
	v_cmp_ne_u32_e32 vcc, v0, v2
	s_cbranch_vccnz .LBB0_669
	s_cmp_gt_i32 s89, 5
	s_cselect_b64 s[0:1], -1, 0
	s_lshl_b32 s2, s89, 3
	s_add_i32 s3, 0, 0x20174
	s_add_i32 s10, s2, 0
	v_add_u32_e32 v3, 1, v2
	s_mov_b32 s28, 0
	v_mov_b32_e32 v4, s3
	s_add_i32 s2, s10, 0x20180
	v_mov_b32_e32 v1, 0
	s_mov_b32 s3, 0x10000
	v_mov_b32_e32 v5, 0x10001
	s_add_i32 s10, s10, 0x20184
	s_movk_i32 s11, 0x4000
	s_mov_b32 s12, 0x8000
	s_mov_b32 s13, 0xc000
	s_mov_b32 s14, 0x14000
	s_mov_b32 s15, 0x18000
	s_mov_b32 s16, 0x1c000
	s_mov_b32 s17, 0x20000
	s_mov_b32 s18, 0x24000
	s_mov_b32 s19, 0x28000
	s_mov_b32 s20, 0x2c000
	s_mov_b32 s21, 0x30000
	s_mov_b32 s22, 0x34000
	s_mov_b32 s23, 0x38000
	s_mov_b32 s24, 0x3c000
	s_mov_b32 s25, 0xc3e00000
	s_movk_i32 s26, 0x1000
	s_add_i32 s27, 0, 0x20170
	v_mov_b32_e32 v6, 0x43e00000
	s_branch .LBB0_648

; __device__ __forceinline__ void xcd_barrier_cv(const XcdBarrier& b, const CvWork& w) {
;     asm volatile("s_waitcnt vmcnt(0)" ::: "memory");
;     const unsigned g0 = w.rel[0];
;     __syncthreads();
;     if (b.wave == 0) {
;         xb_wave0(b, w.rel + 1, g0 + 1u);
;         w.rel[0] = g0 + 1u;
;     } else if (b.wave != 0) {
;         unsigned guard = 0;
;         while (w.rel[0] == g0) { if (w.rel[1] == g0 + 1u || b.wave > 4) { __builtin_amdgcn_s_sleep(1); continue; }
;             if (!cv_one(w)) __builtin_amdgcn_s_sleep(4); if (++guard > (1u << 22)) break; }
.LBB0_896:
	s_cmp_lt_i32 s81, 6
	s_cbranch_scc1 .LBB0_968
	s_add_i32 s0, 0, 0x20170
	s_waitcnt vmcnt(0)
	v_mov_b32_e32 v0, s0
	ds_read_b32 v2, v0
	s_cmp_eq_u32 s89, 0
	s_waitcnt vmcnt(0) lgkmcnt(0)
	s_barrier
	s_cbranch_scc1 .LBB0_923
	v_mov_b32_e32 v0, s0
	ds_read_b32 v0, v0
	s_waitcnt lgkmcnt(0)
	v_cmp_ne_u32_e32 vcc, v0, v2
	s_cbranch_vccnz .LBB0_922
	s_cmp_gt_i32 s89, 5
	s_cselect_b64 s[0:1], -1, 0
	s_lshl_b32 s2, s89, 3
	s_add_i32 s3, 0, 0x20174
	s_add_i32 s10, s2, 0
	v_add_u32_e32 v3, 1, v2
	s_mov_b32 s28, 0
	v_mov_b32_e32 v4, s3
	s_add_i32 s2, s10, 0x20180
	v_mov_b32_e32 v1, 0
	s_mov_b32 s3, 0x10000
	v_mov_b32_e32 v5, 0x10001
	s_add_i32 s10, s10, 0x20184
	s_movk_i32 s11, 0x4000
	s_mov_b32 s12, 0x8000
	s_mov_b32 s13, 0xc000
	s_mov_b32 s14, 0x14000
	s_mov_b32 s15, 0x18000
	s_mov_b32 s16, 0x1c000
	s_mov_b32 s17, 0x20000
	s_mov_b32 s18, 0x24000
	s_mov_b32 s19, 0x28000
	s_mov_b32 s20, 0x2c000
	s_mov_b32 s21, 0x30000
	s_mov_b32 s22, 0x34000
	s_mov_b32 s23, 0x38000
	s_mov_b32 s24, 0x3c000
	s_mov_b32 s25, 0xc3e00000
	s_movk_i32 s26, 0x1000
	s_add_i32 s27, 0, 0x20170
	v_mov_b32_e32 v6, 0x43e00000
	s_branch .LBB0_901

; __device__ __forceinline__ void xcd_barrier_cv(const XcdBarrier& b, const CvWork& w) {
;     asm volatile("s_waitcnt vmcnt(0)" ::: "memory");
;     const unsigned g0 = w.rel[0];
;     __syncthreads();
;     if (b.wave == 0) {
;         xb_wave0(b, w.rel + 1, g0 + 1u);
;         w.rel[0] = g0 + 1u;
;     } else if (b.wave != 0) {
;         unsigned guard = 0;
;         while (w.rel[0] == g0) { if (w.rel[1] == g0 + 1u || b.wave > 4) { __builtin_amdgcn_s_sleep(1); continue; }
;             if (!cv_one(w)) __builtin_amdgcn_s_sleep(4); if (++guard > (1u << 22)) break; }
.LBB0_972:
	s_cmp_lt_u32 s81, 7
	s_cbranch_scc1 .LBB0_1044
	s_add_i32 s0, 0, 0x20170
	s_waitcnt vmcnt(0)
	v_mov_b32_e32 v0, s0
	ds_read_b32 v2, v0
	s_cmp_eq_u32 s89, 0
	s_waitcnt lgkmcnt(0)
	s_barrier
	s_cbranch_scc1 .LBB0_999
	v_mov_b32_e32 v0, s0
	ds_read_b32 v0, v0
	s_waitcnt lgkmcnt(0)
	v_cmp_ne_u32_e32 vcc, v0, v2
	s_cbranch_vccnz .LBB0_998
	s_cmp_gt_i32 s89, 5
	s_cselect_b64 s[0:1], -1, 0
	s_lshl_b32 s2, s89, 3
	s_add_i32 s3, 0, 0x20174
	s_add_i32 s10, s2, 0
	v_add_u32_e32 v3, 1, v2
	s_mov_b32 s28, 0
	v_mov_b32_e32 v4, s3
	s_add_i32 s2, s10, 0x20180
	v_mov_b32_e32 v1, 0
	s_mov_b32 s3, 0x10000
	v_mov_b32_e32 v5, 0x10001
	s_add_i32 s10, s10, 0x20184
	s_movk_i32 s11, 0x4000
	s_mov_b32 s12, 0x8000
	s_mov_b32 s13, 0xc000
	s_mov_b32 s14, 0x14000
	s_mov_b32 s15, 0x18000
	s_mov_b32 s16, 0x1c000
	s_mov_b32 s17, 0x20000
	s_mov_b32 s18, 0x24000
	s_mov_b32 s19, 0x28000
	s_mov_b32 s20, 0x2c000
	s_mov_b32 s21, 0x30000
	s_mov_b32 s22, 0x34000
	s_mov_b32 s23, 0x38000
	s_mov_b32 s24, 0x3c000
	s_mov_b32 s25, 0xc3e00000
	s_movk_i32 s26, 0x1000
	s_add_i32 s27, 0, 0x20170
	v_mov_b32_e32 v6, 0x43e00000
	s_branch .LBB0_977

; __device__ __forceinline__ void xcd_barrier_cv(const XcdBarrier& b, const CvWork& w) {
;     asm volatile("s_waitcnt vmcnt(0)" ::: "memory");
;     const unsigned g0 = w.rel[0];
;     __syncthreads();
;     if (b.wave == 0) {
;         xb_wave0(b, w.rel + 1, g0 + 1u);
;         w.rel[0] = g0 + 1u;
;     } else if (b.wave != 0) {
;         unsigned guard = 0;
;         while (w.rel[0] == g0) { if (w.rel[1] == g0 + 1u || b.wave > 4) { __builtin_amdgcn_s_sleep(1); continue; }
;             if (!cv_one(w)) __builtin_amdgcn_s_sleep(4); if (++guard > (1u << 22)) break; }
.LBB0_1090:
	s_add_i32 s0, 0, 0x20170
	s_waitcnt vmcnt(0)
	v_mov_b32_e32 v0, s0
	ds_read_b32 v2, v0
	s_cmp_eq_u32 s89, 0
	s_waitcnt lgkmcnt(0)
	s_barrier
	s_cbranch_scc1 .LBB0_1116
	v_mov_b32_e32 v0, s0
	ds_read_b32 v0, v0
	s_waitcnt lgkmcnt(0)
	v_cmp_ne_u32_e32 vcc, v0, v2
	s_cbranch_vccnz .LBB0_1115
	s_cmp_gt_i32 s89, 5
	s_cselect_b64 s[0:1], -1, 0
	s_lshl_b32 s2, s89, 3
	s_add_i32 s3, 0, 0x20174
	s_add_i32 s10, s2, 0
	v_add_u32_e32 v3, 1, v2
	s_mov_b32 s28, 0
	v_mov_b32_e32 v4, s3
	s_add_i32 s2, s10, 0x20180
	v_mov_b32_e32 v1, 0
	s_mov_b32 s3, 0x10000
	v_mov_b32_e32 v5, 0x10001
	s_add_i32 s10, s10, 0x20184
	s_movk_i32 s11, 0x4000
	s_mov_b32 s12, 0x8000
	s_mov_b32 s13, 0xc000
	s_mov_b32 s14, 0x14000
	s_mov_b32 s15, 0x18000
	s_mov_b32 s16, 0x1c000
	s_mov_b32 s17, 0x20000
	s_mov_b32 s18, 0x24000
	s_mov_b32 s19, 0x28000
	s_mov_b32 s20, 0x2c000
	s_mov_b32 s21, 0x30000
	s_mov_b32 s22, 0x34000
	s_mov_b32 s23, 0x38000
	s_mov_b32 s24, 0x3c000
	s_mov_b32 s25, 0xc3e00000
	s_movk_i32 s26, 0x1000
	s_add_i32 s27, 0, 0x20170
	v_mov_b32_e32 v6, 0x43e00000
	s_branch .LBB0_1094

; __device__ __forceinline__ void xcd_barrier_cv(const XcdBarrier& b, const CvWork& w) {
;     asm volatile("s_waitcnt vmcnt(0)" ::: "memory");
;     const unsigned g0 = w.rel[0];
;     __syncthreads();
;     if (b.wave == 0) {
;         xb_wave0(b, w.rel + 1, g0 + 1u);
;         w.rel[0] = g0 + 1u;
;     } else if (b.wave != 0) {
;         unsigned guard = 0;
;         while (w.rel[0] == g0) { if (w.rel[1] == g0 + 1u || b.wave > 4) { __builtin_amdgcn_s_sleep(1); continue; }
;             if (!cv_one(w)) __builtin_amdgcn_s_sleep(4); if (++guard > (1u << 22)) break; }
.LBB0_1217:
	s_cmp_lt_i32 s81, 9
	s_cbranch_scc1 .LBB0_1289
	s_add_i32 s0, 0, 0x20170
	s_waitcnt vmcnt(0)
	v_mov_b32_e32 v0, s0
	ds_read_b32 v2, v0
	s_cmp_eq_u32 s89, 0
	s_waitcnt vmcnt(0) lgkmcnt(0)
	s_barrier
	s_cbranch_scc1 .LBB0_1244
	v_mov_b32_e32 v0, s0
	ds_read_b32 v0, v0
	s_waitcnt lgkmcnt(0)
	v_cmp_ne_u32_e32 vcc, v0, v2
	s_cbranch_vccnz .LBB0_1243
	s_cmp_gt_i32 s89, 5
	s_cselect_b64 s[0:1], -1, 0
	s_lshl_b32 s2, s89, 3
	s_add_i32 s3, 0, 0x20174
	s_add_i32 s10, s2, 0
	v_add_u32_e32 v3, 1, v2
	s_mov_b32 s28, 0
	v_mov_b32_e32 v4, s3
	s_add_i32 s2, s10, 0x20180
	v_mov_b32_e32 v1, 0
	s_mov_b32 s3, 0x10000
	v_mov_b32_e32 v5, 0x10001
	s_add_i32 s10, s10, 0x20184
	s_movk_i32 s11, 0x4000
	s_mov_b32 s12, 0x8000
	s_mov_b32 s13, 0xc000
	s_mov_b32 s14, 0x14000
	s_mov_b32 s15, 0x18000
	s_mov_b32 s16, 0x1c000
	s_mov_b32 s17, 0x20000
	s_mov_b32 s18, 0x24000
	s_mov_b32 s19, 0x28000
	s_mov_b32 s20, 0x2c000
	s_mov_b32 s21, 0x30000
	s_mov_b32 s22, 0x34000
	s_mov_b32 s23, 0x38000
	s_mov_b32 s24, 0x3c000
	s_mov_b32 s25, 0xc3e00000
	s_movk_i32 s26, 0x1000
	s_add_i32 s27, 0, 0x20170
	v_mov_b32_e32 v6, 0x43e00000
	s_branch .LBB0_1222

; __device__ __forceinline__ int lane_id_now() { unsigned z = 0u; asm volatile("" : "+v"(z)); return (int)__builtin_amdgcn_mbcnt_hi(~0u, __builtin_amdgcn_mbcnt_lo(~0u, z)); }
; __device__ __forceinline__ bool cv_one(const CvWork& w) {
;     if (w.wave == 0) return false;
;     int it = __builtin_amdgcn_readfirstlane(w.cur[2 * w.wave]); const int end = __builtin_amdgcn_readfirstlane(w.cur[2 * w.wave + 1]);
;     if (it >= end) {
;         if (it > CV_ITEMS) return false;
;         unsigned base = 0u; if (lane_id_now() == 0) base = __hip_atomic_fetch_add(w.q, (unsigned)CV_BATCH, __ATOMIC_RELAXED, __HIP_MEMORY_SCOPE_AGENT);
;         base = __builtin_amdgcn_readfirstlane(base);
;         if (base >= (unsigned)CV_ITEMS) { w.cur[2 * w.wave] = CV_ITEMS + 1; w.cur[2 * w.wave + 1] = 0; return false; }
;         it = (int)base; w.cur[2 * w.wave + 1] = (int)base + CV_BATCH;
;     }
;     TItem d; { int r = it; const int e = r / CV_I_UP; r -= e * CV_I_UP; const int nb_ = 2 * FF / 32, kb = r / nb_, nbi = r % nb_;
;         d.src = w.wup + (size_t)e * D * 2 * FF + (size_t)(128 * kb) * (2 * FF) + 32 * nbi; d.dst = (bf16*)(w.wup8 + (size_t)e * 2 * FF * D + (size_t)(32 * nbi) * D + 128 * kb);
;         d.gain = w.gain + 128 * kb; d.N = 2 * FF; d.ldk = D; }
;     const int lane = lane_id_now();
;     f32x4 r[16], g[4]; titem8_load<true, true>(d, lane, r, g); titem8_store<true, true>(d, lane, r, g);
;     w.cur[2 * w.wave] = it + 1;
;     return true;
; }
; __device__ __forceinline__ void cv_flush(const CvWork& w) { while (cv_one(w)) {} }
.LBB0_1413:
	s_cmp_eq_u32 s89, 0
	s_cselect_b64 s[0:1], -1, 0
	s_and_b64 vcc, exec, s[0:1]
	s_cbranch_vccnz .LBB0_1430
	s_cmp_gt_u32 s89, 5
	s_cbranch_scc1 .LBB0_1430
	s_lshl_b32 s2, s89, 3
	s_add_i32 s3, s2, 0
	s_add_i32 s2, s3, 0x20180
	v_mov_b32_e32 v2, s2
	s_waitcnt lgkmcnt(0)
	v_mov_b32_e32 v1, 0
	s_mov_b32 s2, 0x10000
	v_mov_b32_e32 v3, 0x10001
	s_add_i32 s3, s3, 0x20184
	s_movk_i32 s12, 0x4000
	s_mov_b32 s13, 0x8000
	s_mov_b32 s14, 0xc000
	s_mov_b32 s15, 0x14000
	s_mov_b32 s16, 0x18000
	s_mov_b32 s17, 0x1c000
	s_mov_b32 s18, 0x20000
	s_mov_b32 s19, 0x24000
	s_mov_b32 s20, 0x28000
	s_mov_b32 s21, 0x2c000
	s_mov_b32 s22, 0x30000
	s_mov_b32 s23, 0x34000
	s_mov_b32 s24, 0x38000
	s_mov_b32 s25, 0x3c000
	s_mov_b32 s26, 0xc3e00000
	s_movk_i32 s27, 0x1000
	v_mov_b32_e32 v4, 0x43e00000
	s_branch .LBB0_1416
